# speedup vs baseline: 1.0152x; 1.0031x over previous
_Z8gemm_f16ILi128ELi64ELi2ELi2ELi4ELi2ELi0EEvPKDF16_S1_Pviiii:
	s_load_dwordx4 s[4:7], s[0:1], 0x0
	s_load_dwordx2 s[8:9], s[0:1], 0x10
	s_and_b32 s3, s2, 7
	s_lshr_b32 s10, s2, 3
	s_lshr_b32 s11, s3, 1
	s_lshl_b32 s11, s11, 2
	s_and_b32 s12, s10, 3
	s_and_b32 s3, s3, 1
	s_lshl_b32 s3, s3, 3
	s_lshr_b32 s10, s10, 2
	s_add_i32 s10, s10, s3
	s_add_i32 s3, s11, s12
	s_mov_b32 s11, s10
	s_lshl_b32 s10, s3, 7
	s_lshl_b32 s11, s11, 6
	v_lshrrev_b32_e32 v13, 3, v0
	v_and_b32_e32 v14, 7, v0
	v_bfe_u32 v15, v0, 4, 3
	v_xor_b32_e32 v14, v14, v15
	v_lshlrev_b32_e32 v14, 4, v14
	v_add_u32_e32 v15, s10, v13
	v_mul_u32_u24_e32 v15, 0xc00, v15
	v_add_u32_e32 v3, v15, v14
	v_add_u32_e32 v4, 0x18000, v3
	v_add_u32_e32 v5, 0x30000, v3
	v_add_u32_e32 v6, 0x48000, v3
	v_add_u32_e32 v15, s11, v13
	v_mul_u32_u24_e32 v15, 0xc00, v15
	v_add_u32_e32 v7, v15, v14
	v_add_u32_e32 v8, 0x18000, v7
	v_lshlrev_b32_e32 v13, 4, v0
	s_nop 0
	v_readfirstlane_b32 s20, v13
	v_and_b32_e32 v13, 15, v0
	v_bfe_u32 v14, v0, 4, 2
	v_bfe_u32 v15, v0, 1, 3
	v_xor_b32_e32 v14, v14, v15
	v_lshlrev_b32_e32 v14, 4, v14
	v_lshl_or_b32 v14, v13, 7, v14
	v_lshrrev_b32_e32 v13, 7, v0
	v_lshl_or_b32 v1, v13, 13, v14
	v_bfe_u32 v13, v0, 6, 1
	v_lshlrev_b32_e32 v13, 12, v13
	v_or_b32_e32 v13, 0x4000, v13
	v_or_b32_e32 v2, v13, v14
	s_waitcnt lgkmcnt(0)
	s_mov_b32 s14, s4
	s_mov_b32 s15, s5
	s_mov_b32 s16, s6
	s_mov_b32 s17, s7
	s_mov_b32 s21, s20
	s_mov_b32 m0, s21
	s_add_i32 s21, s21, 0x1000
	global_load_lds_dwordx4 v3, s[14:15]
	s_mov_b32 m0, s21
	s_add_i32 s21, s21, 0x1000
	global_load_lds_dwordx4 v4, s[14:15]
	s_mov_b32 m0, s21
	s_add_i32 s21, s21, 0x1000
	global_load_lds_dwordx4 v5, s[14:15]
	s_mov_b32 m0, s21
	s_add_i32 s21, s21, 0x1000
	global_load_lds_dwordx4 v6, s[14:15]
	s_mov_b32 m0, s21
	s_add_i32 s21, s21, 0x1000
	global_load_lds_dwordx4 v7, s[16:17]
	s_mov_b32 m0, s21
	s_add_i32 s21, s21, 0x1000
	global_load_lds_dwordx4 v8, s[16:17]
	s_add_u32 s14, s14, 0x80
	s_addc_u32 s15, s15, 0
	s_add_u32 s16, s16, 0x80
	s_addc_u32 s17, s17, 0
	s_mov_b32 m0, s21
	s_add_i32 s21, s21, 0x1000
	global_load_lds_dwordx4 v3, s[14:15]
	s_mov_b32 m0, s21
	s_add_i32 s21, s21, 0x1000
	global_load_lds_dwordx4 v4, s[14:15]
	s_mov_b32 m0, s21
	s_add_i32 s21, s21, 0x1000
	global_load_lds_dwordx4 v5, s[14:15]
	s_mov_b32 m0, s21
	s_add_i32 s21, s21, 0x1000
	global_load_lds_dwordx4 v6, s[14:15]
	s_mov_b32 m0, s21
	s_add_i32 s21, s21, 0x1000
	global_load_lds_dwordx4 v7, s[16:17]
	s_mov_b32 m0, s21
	s_add_i32 s21, s21, 0x1000
	global_load_lds_dwordx4 v8, s[16:17]
	s_add_u32 s14, s14, 0x80
	s_addc_u32 s15, s15, 0
	s_add_u32 s16, s16, 0x80
	s_addc_u32 s17, s17, 0
	s_mov_b32 m0, s21
	s_add_i32 s21, s21, 0x1000
	global_load_lds_dwordx4 v3, s[14:15]
	s_mov_b32 m0, s21
	s_add_i32 s21, s21, 0x1000
	global_load_lds_dwordx4 v4, s[14:15]
	s_mov_b32 m0, s21
	s_add_i32 s21, s21, 0x1000
	global_load_lds_dwordx4 v5, s[14:15]
	s_mov_b32 m0, s21
	s_add_i32 s21, s21, 0x1000
	global_load_lds_dwordx4 v6, s[14:15]
	s_mov_b32 m0, s21
	s_add_i32 s21, s21, 0x1000
	global_load_lds_dwordx4 v7, s[16:17]
	s_mov_b32 m0, s21
	s_add_i32 s21, s21, 0x1000
	global_load_lds_dwordx4 v8, s[16:17]
	s_add_u32 s14, s14, 0x80
	s_addc_u32 s15, s15, 0
	s_add_u32 s16, s16, 0x80
	s_addc_u32 s17, s17, 0
	s_mov_b32 m0, s21
	s_add_i32 s21, s21, 0x1000
	global_load_lds_dwordx4 v3, s[14:15]
	s_mov_b32 m0, s21
	s_add_i32 s21, s21, 0x1000
	global_load_lds_dwordx4 v4, s[14:15]
	s_mov_b32 m0, s21
	s_add_i32 s21, s21, 0x1000
	global_load_lds_dwordx4 v5, s[14:15]
	s_mov_b32 m0, s21
	s_add_i32 s21, s21, 0x1000
	global_load_lds_dwordx4 v6, s[14:15]
	s_mov_b32 m0, s21
	s_add_i32 s21, s21, 0x1000
	global_load_lds_dwordx4 v7, s[16:17]
	s_mov_b32 m0, s21
	s_add_i32 s21, s21, 0x1000
	global_load_lds_dwordx4 v8, s[16:17]
	v_accvgpr_write_b32 a0, 0
	v_accvgpr_write_b32 a1, 0
	v_accvgpr_write_b32 a2, 0
	v_accvgpr_write_b32 a3, 0
	v_accvgpr_write_b32 a4, 0
	v_accvgpr_write_b32 a5, 0
	v_accvgpr_write_b32 a6, 0
	v_accvgpr_write_b32 a7, 0
	v_accvgpr_write_b32 a8, 0
	v_accvgpr_write_b32 a9, 0
	v_accvgpr_write_b32 a10, 0
	v_accvgpr_write_b32 a11, 0
	v_accvgpr_write_b32 a12, 0
	v_accvgpr_write_b32 a13, 0
	v_accvgpr_write_b32 a14, 0
	v_accvgpr_write_b32 a15, 0
	v_accvgpr_write_b32 a16, 0
	v_accvgpr_write_b32 a17, 0
	v_accvgpr_write_b32 a18, 0
	v_accvgpr_write_b32 a19, 0
	v_accvgpr_write_b32 a20, 0
	v_accvgpr_write_b32 a21, 0
	v_accvgpr_write_b32 a22, 0
	v_accvgpr_write_b32 a23, 0
	v_accvgpr_write_b32 a24, 0
	v_accvgpr_write_b32 a25, 0
	v_accvgpr_write_b32 a26, 0
	v_accvgpr_write_b32 a27, 0
	v_accvgpr_write_b32 a28, 0
	v_accvgpr_write_b32 a29, 0
	v_accvgpr_write_b32 a30, 0
	v_accvgpr_write_b32 a31, 0
	s_mov_b32 s12, 0
	s_mov_b32 s13, 0
	v_mov_b32_e32 v9, v1
	v_mov_b32_e32 v11, v2
	v_xor_b32_e32 v10, 64, v1
	v_xor_b32_e32 v12, 64, v2
	s_waitcnt vmcnt(18)
	s_barrier
	ds_read_b128 v[16:19], v11
	ds_read_b128 v[24:27], v9
	ds_read_b128 v[20:23], v11 offset:2048
	ds_read_b128 v[28:31], v9 offset:2048
	ds_read_b128 v[32:35], v9 offset:4096
	ds_read_b128 v[36:39], v9 offset:6144
